# speedup vs baseline: 1.0065x; 1.0065x over previous
_Z11prep_kernelPKfS0_S0_S0_S0_PDF16_S1_S1_P15HIP_vector_typeIfLj2EE:
	s_load_dwordx8 s[4:11], s[0:1], 0x28
	s_mov_b32 s3, 0xfffffe00
	s_cmpk_lt_u32 s2, 0x200
	s_cselect_b32 s3, 0x1000, s3
	s_add_i32 s2, s2, s3
	s_cmpk_gt_i32 s2, 0x7ff
	s_mov_b64 s[12:13], -1
	s_cbranch_scc1 .LBB0_3
	s_andn2_b64 vcc, exec, s[12:13]
	s_cbranch_vccz .LBB0_12

_Z10attn64_fwdPKDF16_S0_S0_PDF16_:
	s_bfe_u32 s3, s2, 0x40003
	s_lshl_b32 s27, s3, 1
	v_readfirstlane_b32 s19, v0
	s_xor_b32 s28, s27, 31
	s_cmpk_lt_u32 s19, 0x100
	s_cselect_b64 s[4:5], -1, 0
	s_and_b64 s[4:5], s[4:5], exec
	s_cselect_b32 s29, s28, 0x63
	s_sub_i32 s8, 34, s27
	v_sub_co_u32_e64 v1, s[4:5], 3, s29
	s_and_b64 s[4:5], s[4:5], exec
	v_readfirstlane_b32 s4, v1
	s_cselect_b32 s9, 3, s4
	s_cmpk_lt_u32 s19, 0x100
	s_cselect_b64 s[4:5], -1, 0
	s_and_b64 s[4:5], s[4:5], exec
	v_sub_co_u32_e64 v1, s[6:7], 2, s29
	s_cselect_b32 s18, s9, s8
	s_sub_i32 s8, 33, s27
	s_and_b64 s[4:5], s[6:7], exec
	v_readfirstlane_b32 s4, v1
	s_cselect_b32 s6, 2, s4
	s_cmpk_lt_u32 s19, 0x100
	s_cselect_b64 s[4:5], -1, 0
	s_and_b64 s[4:5], s[4:5], exec
	s_cselect_b32 s24, s6, s8
	s_sub_i32 s4, 32, s27
	s_cmp_lg_u32 s29, 1
	s_cselect_b64 s[6:7], -1, 0
	s_cmpk_lt_u32 s19, 0x100
	v_cndmask_b32_e64 v2, 0, 1, s[6:7]
	s_cselect_b64 s[6:7], -1, 0
	s_load_dwordx8 s[8:15], s[0:1], 0x0
	s_mul_i32 s16, s28, 0x11000
	s_and_b64 s[0:1], s[6:7], exec
	s_cselect_b32 s23, 0, s16
	s_lshr_b32 s1, s2, 4
	s_and_b32 s0, s2, 7
	s_and_b32 s1, s1, 0x3fffff8
	s_or_b32 s2, s1, s0
	s_lshr_b32 s0, s19, 8
	v_mov_b32_e32 v3, s4
	s_mul_i32 s1, s0, 0xc000
	s_bfe_u32 s0, s19, 0x20006
	s_lshl_b32 s4, s2, 6
	s_lshr_b32 s2, s19, 4
	s_mov_b32 s5, 0
	v_cndmask_b32_e64 v6, v3, v2, s[6:7]
	s_lshl_b32 s3, s3, 7
	s_lshl_b32 s16, s0, 5
	v_and_b32_e32 v3, 7, v0
	s_and_b32 s2, s2, 4
	v_bfe_u32 v4, v0, 4, 2
	s_or_b32 s17, s16, s3
	s_add_i32 s22, s1, 0
	s_and_b32 s1, s19, 0x3fffffc0
	v_bitop3_b32 v4, s2, v3, v4 bitop3:0x36
	s_lshl_b64 s[2:3], s[4:5], 1
	s_waitcnt lgkmcnt(0)
	s_add_u32 s20, s12, s2
	s_addc_u32 s21, s13, s3
	s_lshl_b32 s4, s0, 10
	s_add_i32 s30, s4, s22
	v_bfe_u32 v226, v0, 3, 3
	s_cmpk_gt_u32 s19, 0xff
	v_lshl_or_b32 v2, s0, 3, v226
	s_cselect_b64 s[12:13], -1, 0
	s_xor_b32 s25, s17, 0xf80
	v_mul_u32_u24_e32 v2, 0x440, v2
	s_add_u32 s10, s10, s2
	v_lshlrev_b32_e32 v35, 1, v0
	v_lshlrev_b32_e32 v227, 3, v3
	s_addc_u32 s11, s11, s3
	v_lshlrev_b32_e32 v126, 1, v2
	v_mov_b32_e32 v127, 0
	v_bitop3_b32 v7, v35, v227, 32 bitop3:0x6c
	v_lshl_add_u64 v[2:3], s[10:11], 0, v[126:127]
	v_lshlrev_b32_e32 v4, 4, v4
	v_mov_b32_e32 v5, v127
	v_lshl_add_u64 v[222:223], v[2:3], 0, v[4:5]
	v_lshl_add_u64 v[2:3], s[20:21], 0, v[126:127]
	v_lshlrev_b32_e32 v126, 1, v7
	s_lshl_b32 s4, s23, 1
	v_lshl_add_u64 v[224:225], v[2:3], 0, v[126:127]
	v_lshl_add_u64 v[2:3], v[222:223], 0, s[4:5]
	s_mov_b32 m0, s30
	s_nop 0
	global_load_lds_dwordx4 v[2:3], off
	s_mov_b64 s[10:11], 0x11000
	v_lshl_add_u64 v[2:3], v[2:3], 0, s[10:11]
	s_add_i32 s19, s30, 0x1000
	s_mov_b32 m0, s19
	s_nop 0
	global_load_lds_dwordx4 v[2:3], off
	s_add_i32 s31, s30, 0x6000
	v_lshl_add_u64 v[2:3], v[224:225], 0, s[4:5]
	s_mov_b32 m0, s31
	s_nop 0
	global_load_lds_dwordx4 v[2:3], off
	s_add_i32 s4, s31, 0x1000
	v_lshl_add_u64 v[2:3], v[2:3], 0, s[10:11]
	s_mov_b32 m0, s4
	s_nop 0
	global_load_lds_dwordx4 v[2:3], off
	s_mov_b32 s4, 0x22000
	v_mul_lo_u32 v126, v6, s4
	s_add_i32 s4, s30, 0x2000
	v_lshl_add_u64 v[2:3], v[222:223], 0, v[126:127]
	s_mov_b32 m0, s4
	s_nop 0
	global_load_lds_dwordx4 v[2:3], off
	s_add_i32 s4, s30, 0x3000
	s_mul_i32 s23, s25, 0x440
	v_lshl_add_u64 v[2:3], v[2:3], 0, s[10:11]
	s_mov_b32 m0, s4
	s_nop 0
	global_load_lds_dwordx4 v[2:3], off
	s_lshl_b32 s4, s23, 1
	s_add_u32 s4, s8, s4
	v_and_b32_e32 v228, 31, v0
	v_bfe_u32 v1, v0, 5, 1
	s_addc_u32 s21, s9, 0
	s_add_u32 s20, s4, s2
	v_mul_u32_u24_e32 v2, 0x440, v228
	v_lshlrev_b32_e32 v233, 4, v1
	s_addc_u32 s21, s21, s3
	v_lshl_or_b32 v34, v2, 1, v233
	global_load_dwordx4 v[146:149], v34, s[20:21]
	global_load_dwordx4 v[150:153], v34, s[20:21] offset:32
	global_load_dwordx4 v[154:157], v34, s[20:21] offset:64
	global_load_dwordx4 v[158:161], v34, s[20:21] offset:96
	v_lshrrev_b32_e32 v2, 1, v0
	v_lshl_add_u32 v44, v228, 7, s22
	v_bitop3_b32 v2, v1, v2, 7 bitop3:0x78
	s_mul_i32 s20, s24, 0x11000
	v_lshl_add_u32 v234, v2, 4, v44
	v_mov_b32_e32 v2, v127
	v_mov_b32_e32 v3, v127
	v_mov_b32_e32 v4, v127
	v_mov_b32_e32 v6, v127
	v_mov_b32_e32 v7, v127
	v_mov_b32_e32 v8, v127
	v_mov_b32_e32 v9, v127
	v_mov_b32_e32 v10, v127
	v_mov_b32_e32 v11, v127
	v_mov_b32_e32 v12, v127
	v_mov_b32_e32 v13, v127
	v_mov_b32_e32 v14, v127
	v_mov_b32_e32 v15, v127
	v_mov_b32_e32 v16, v127
	v_mov_b32_e32 v17, v127
	s_ashr_i32 s21, s20, 31
	v_lshl_add_u64 v[18:19], s[20:21], 1, v[222:223]
	s_add_i32 s4, s30, 0x4000
	s_mov_b32 m0, s4
	s_nop 0
	global_load_lds_dwordx4 v[18:19], off
	v_lshl_add_u64 v[18:19], v[18:19], 0, s[10:11]
	s_add_i32 s4, s30, 0x5000
	s_mov_b32 m0, s4
	s_nop 0
	global_load_lds_dwordx4 v[18:19], off
	s_waitcnt vmcnt(6) lgkmcnt(0)
	s_barrier
	ds_read_b128 v[36:39], v234
	ds_read_b128 v[40:43], v234 offset:4096
	s_waitcnt vmcnt(3) lgkmcnt(1)
	v_mfma_f32_32x32x16_f16 v[18:33], v[36:39], v[146:149], v[2:17]
	v_bfe_u32 v45, v0, 1, 3
	v_bitop3_b32 v36, v1, v45, 2 bitop3:0x36
	v_lshl_add_u32 v235, v36, 4, v44
	v_lshlrev_b32_e32 v229, 9, v1
	s_mul_i32 s20, s18, 0x11000
	s_ashr_i32 s21, s20, 31
	s_lshl_b32 s1, s1, 2
	s_waitcnt lgkmcnt(0)
	v_mfma_f32_32x32x16_f16 v[2:17], v[40:43], v[146:149], v[2:17]
	ds_read_b128 v[36:39], v235
	ds_read_b128 v[40:43], v235 offset:4096
	s_add_i32 s24, s1, 0
	s_lshl_b32 s25, s0, 11
	s_lshl_b32 s1, s0, 13
	s_lshl_b32 s0, s0, 8
	s_add_i32 s1, s1, 0
	s_add_i32 s0, s0, 0
	s_waitcnt vmcnt(2) lgkmcnt(1)
	v_mfma_f32_32x32x16_f16 v[18:33], v[36:39], v[150:153], v[18:33]
	v_bitop3_b32 v36, v1, v45, 4 bitop3:0x36
	v_lshl_add_u32 v236, v36, 4, v44
	s_add_i32 s24, s24, 0x18000
	s_mul_i32 s26, s17, 0x440
	v_lshlrev_b32_e32 v230, 2, v1
	s_mov_b32 s38, 1
	s_movk_i32 s35, 0x2000
	s_waitcnt lgkmcnt(0)
	v_mfma_f32_32x32x16_f16 v[2:17], v[40:43], v[150:153], v[2:17]
	ds_read_b128 v[36:39], v236
	ds_read_b128 v[40:43], v236 offset:4096
	s_movk_i32 s36, 0x4000
	s_mov_b32 s34, 0x41000000
	v_or_b32_e32 v241, s16, v228
	v_or_b32_e32 v242, 0xfffff840, v230
	v_or_b32_e32 v243, 0xfffff880, v230
	v_mov_b32_e32 v244, 0x22000
	s_waitcnt vmcnt(1) lgkmcnt(1)
	v_mfma_f32_32x32x16_f16 v[18:33], v[36:39], v[154:157], v[18:33]
	v_bitop3_b32 v36, v1, v45, 6 bitop3:0x36
	v_lshl_add_u32 v237, v36, 4, v44
	v_mov_b32_e32 v245, 0xff800000
	v_mov_b32_e32 v246, v127
	v_mov_b32_e32 v247, v127
	s_waitcnt lgkmcnt(0)
	v_mfma_f32_32x32x16_f16 v[2:17], v[40:43], v[154:157], v[2:17]
	ds_read_b128 v[36:39], v237
	ds_read_b128 v[40:43], v237 offset:4096
	s_waitcnt vmcnt(0) lgkmcnt(1)
	v_mfma_f32_32x32x16_f16 v[18:33], v[36:39], v[158:161], v[18:33]
	s_waitcnt lgkmcnt(0)
	v_mfma_f32_32x32x16_f16 v[2:17], v[40:43], v[158:161], v[2:17]
	s_nop 9
	v_max_f32_e32 v36, v19, v19
	v_max_f32_e32 v37, v18, v18
	v_max_f32_e32 v36, v37, v36
	v_max3_f32 v36, v36, v2, v4
	v_max3_f32 v37, v20, v21, v3
	v_max3_f32 v36, v36, v5, v22
	v_max3_f32 v37, v37, v24, v25
	v_max3_f32 v36, v36, v23, v6
	v_max3_f32 v37, v37, v8, v9
	v_max3_f32 v36, v36, v7, v26
	v_max3_f32 v37, v37, v28, v29
	v_max3_f32 v36, v36, v27, v10
	v_max3_f32 v37, v37, v12, v13
	v_max3_f32 v36, v36, v11, v30
	v_max3_f32 v37, v37, v32, v33
	v_max3_f32 v36, v36, v31, v14
	v_max3_f32 v37, v37, v16, v17
	v_max3_f32 v36, v36, v15, v37
	v_mov_b32_e32 v37, v36
	s_nop 1
	v_permlane32_swap_b32_e32 v36, v37
	v_max_f32_e32 v37, v37, v37
	v_max_f32_e32 v36, v36, v36
	v_max_f32_e32 v248, v36, v37
	v_sub_f32_e32 v39, v3, v248
	v_lshlrev_b32_e32 v3, 5, v0
	v_sub_f32_e32 v38, v2, v248
	v_and_b32_e32 v2, 32, v35
	v_and_b32_e32 v3, 0x180, v3
	v_lshlrev_b32_e32 v35, 3, v0
	v_sub_f32_e32 v40, v4, v248
	v_add3_u32 v3, s22, v229, v3
	v_and_b32_e32 v4, 24, v35
	v_add3_u32 v50, v3, v2, v4
	v_xor_b32_e32 v2, 0x80000000, v248
	v_sub_f32_e32 v41, v5, v248
	v_sub_f32_e32 v42, v6, v248
	v_sub_f32_e32 v43, v7, v248
	v_sub_f32_e32 v44, v8, v248
	v_sub_f32_e32 v45, v9, v248
	v_sub_f32_e32 v46, v10, v248
	v_sub_f32_e32 v47, v11, v248
	v_sub_f32_e32 v48, v12, v248
	v_sub_f32_e32 v49, v13, v248
	v_sub_f32_e32 v62, v14, v248
	v_sub_f32_e32 v63, v15, v248
	v_sub_f32_e32 v64, v16, v248
	v_sub_f32_e32 v65, v17, v248
	v_mov_b32_e32 v3, v2
	v_mov_b32_e32 v4, v2
	v_mov_b32_e32 v5, v2
	v_mov_b32_e32 v6, v2
	v_mov_b32_e32 v7, v2
	v_mov_b32_e32 v8, v2
	v_mov_b32_e32 v9, v2
	v_mov_b32_e32 v10, v2
	v_mov_b32_e32 v11, v2
	v_mov_b32_e32 v12, v2
	v_mov_b32_e32 v13, v2
	v_mov_b32_e32 v14, v2
	v_mov_b32_e32 v15, v2
	v_mov_b32_e32 v16, v2
	v_mov_b32_e32 v17, v2
	s_waitcnt vmcnt(0) lgkmcnt(0)
	s_barrier
	v_sub_f32_e32 v36, v18, v248
	v_sub_f32_e32 v37, v19, v248
	v_lshl_add_u64 v[18:19], s[20:21], 1, v[222:223]
	s_mov_b32 m0, s30
	s_nop 0
	global_load_lds_dwordx4 v[18:19], off
	v_lshl_add_u64 v[18:19], v[18:19], 0, s[10:11]
	s_mov_b32 m0, s19
	s_nop 0
	global_load_lds_dwordx4 v[18:19], off
	s_add_i32 s4, s31, 0x2000
	v_lshl_add_u64 v[18:19], v[224:225], 0, v[126:127]
	s_mov_b32 m0, s4
	s_nop 0
	global_load_lds_dwordx4 v[18:19], off
	v_lshl_add_u64 v[18:19], v[18:19], 0, s[10:11]
	s_add_i32 s4, s31, 0x3000
	s_mov_b32 m0, s4
	s_nop 0
	global_load_lds_dwordx4 v[18:19], off
	ds_read_b128 v[206:209], v234 offset:8192
	ds_read_b128 v[202:205], v234 offset:12288
	ds_read_b128 v[198:201], v235 offset:8192
	ds_read_b128 v[194:197], v235 offset:12288
	ds_read_b128 v[190:193], v236 offset:8192
	ds_read_b128 v[186:189], v236 offset:12288
	ds_read_b128 v[182:185], v237 offset:8192
	ds_read_b128 v[178:181], v237 offset:12288
	s_add_i32 s4, s1, 0x18c00
	s_add_i32 s18, s0, 0x18800
	v_sub_f32_e32 v20, v20, v248
	v_sub_f32_e32 v21, v21, v248
	v_sub_f32_e32 v22, v22, v248
	v_sub_f32_e32 v23, v23, v248
	v_sub_f32_e32 v24, v24, v248
	v_sub_f32_e32 v25, v25, v248
	v_sub_f32_e32 v26, v26, v248
	v_sub_f32_e32 v27, v27, v248
	v_sub_f32_e32 v28, v28, v248
	v_sub_f32_e32 v29, v29, v248
	v_sub_f32_e32 v30, v30, v248
	v_sub_f32_e32 v31, v31, v248
	v_sub_f32_e32 v32, v32, v248
	v_sub_f32_e32 v33, v33, v248
	v_and_b32_e32 v18, 64, v35
	s_add_u32 s8, s8, s2
	v_add_u32_e32 v240, v50, v18
	v_xad_u32 v239, v18, 64, v50
	v_exp_f32_e32 v66, v36
	v_exp_f32_e32 v67, v37
	v_exp_f32_e32 v50, v38
	v_exp_f32_e32 v51, v39
	v_exp_f32_e32 v68, v20
	v_exp_f32_e32 v52, v40
	v_exp_f32_e32 v69, v21
	v_exp_f32_e32 v53, v41
	v_exp_f32_e32 v70, v22
	v_exp_f32_e32 v54, v42
	v_exp_f32_e32 v71, v23
	v_exp_f32_e32 v55, v43
	v_exp_f32_e32 v72, v24
	v_exp_f32_e32 v56, v44
	v_exp_f32_e32 v73, v25
	v_exp_f32_e32 v57, v45
	v_exp_f32_e32 v74, v26
	v_exp_f32_e32 v58, v46
	v_exp_f32_e32 v75, v27
	v_exp_f32_e32 v59, v47
	v_exp_f32_e32 v76, v28
	v_exp_f32_e32 v60, v48
	v_exp_f32_e32 v77, v29
	v_exp_f32_e32 v61, v49
	v_exp_f32_e32 v78, v30
	v_exp_f32_e32 v62, v62
	v_exp_f32_e32 v79, v31
	v_exp_f32_e32 v63, v63
	v_exp_f32_e32 v80, v32
	v_exp_f32_e32 v64, v64
	v_exp_f32_e32 v81, v33
	v_exp_f32_e32 v65, v65
	s_addc_u32 s9, s9, s3
	s_lshl_b32 s17, s26, 1
	v_and_b32_e32 v0, 63, v0
	s_waitcnt vmcnt(4) lgkmcnt(0)
	s_barrier
	s_add_u32 s8, s8, s17
	v_mov_b32_e32 v35, v127
	v_cmp_gt_u32_e64 s[0:1], 32, v0
	s_addc_u32 s9, s9, 0
	v_lshl_add_u32 v232, v0, 2, s4
	v_lshlrev_b32_e32 v0, 2, v228
	v_add_u32_e32 v231, s24, v0
	v_add_u32_e32 v238, s18, v0
	v_lshl_add_u64 v[0:1], s[8:9], 0, v[34:35]
	s_sub_i32 s33, 0, s29
	v_mov_b32_e32 v34, v127
	v_mov_b32_e32 v36, v127
	v_mov_b32_e32 v37, v127
	v_mov_b32_e32 v38, v127
	v_mov_b32_e32 v39, v127
	v_mov_b32_e32 v40, v127
	v_mov_b32_e32 v41, v127
	v_mov_b32_e32 v42, v127
	v_mov_b32_e32 v43, v127
	v_mov_b32_e32 v44, v127
	v_mov_b32_e32 v45, v127
	v_mov_b32_e32 v46, v127
	v_mov_b32_e32 v47, v127
	v_mov_b32_e32 v48, v127
	v_mov_b32_e32 v49, v127
	v_mov_b32_e32 v18, v127
	v_mov_b32_e32 v19, v127
	v_mov_b32_e32 v20, v127
	v_mov_b32_e32 v21, v127
	v_mov_b32_e32 v22, v127
	v_mov_b32_e32 v23, v127
	v_mov_b32_e32 v24, v127
	v_mov_b32_e32 v25, v127
	v_mov_b32_e32 v26, v127
	v_mov_b32_e32 v27, v127
	v_mov_b32_e32 v28, v127
	v_mov_b32_e32 v29, v127
	v_mov_b32_e32 v30, v127
	v_mov_b32_e32 v31, v127
	v_mov_b32_e32 v32, v127
	v_mov_b32_e32 v33, v127
	s_branch .LBB1_2

.LBB1_5:
	v_add_u32_e32 v126, s5, v240
	ds_read_b64_tr_b16 v[122:123], v126 offset:24576
	ds_read_b64_tr_b16 v[124:125], v126 offset:25600
	s_waitcnt lgkmcnt(9)
	v_mfma_f32_32x32x16_f16 v[98:113], v[206:209], v[146:149], v[2:17]
	v_add_f32_e32 v82, v66, v67
	v_mov_b32_e32 v251, v68
	v_add_f32_e32 v82, v69, v82
	v_add_f32_e32 v251, v70, v251
	v_add_f32_e32 v82, v71, v82
	v_cvt_pk_f16_f32 v162, v66, v67
	v_cvt_pk_f16_f32 v163, v68, v69
	v_add_u32_e32 v128, s5, v239
	ds_read_b64_tr_b16 v[118:119], v128 offset:24576
	ds_read_b64_tr_b16 v[120:121], v128 offset:25600
	v_add_f32_e32 v66, v72, v82
	s_waitcnt lgkmcnt(10)
	v_mfma_f32_32x32x16_f16 v[82:97], v[202:205], v[146:149], v[2:17]
	v_add_f32_e32 v251, v73, v251
	v_add_f32_e32 v66, v74, v66
	v_add_f32_e32 v251, v75, v251
	v_cvt_pk_f16_f32 v164, v70, v71
	v_cvt_pk_f16_f32 v165, v72, v73
	ds_read_b64_tr_b16 v[114:115], v126 offset:26624
	ds_read_b64_tr_b16 v[116:117], v126 offset:27648
	s_waitcnt lgkmcnt(11)
	v_mfma_f32_32x32x16_f16 v[98:113], v[198:201], v[150:153], v[98:113]
	v_add_f32_e32 v66, v76, v66
	v_add_f32_e32 v251, v77, v251
	v_add_f32_e32 v66, v78, v66
	v_add_f32_e32 v251, v79, v251
	v_cvt_pk_f16_f32 v166, v74, v75
	v_cvt_pk_f16_f32 v167, v76, v77
	ds_read_b64_tr_b16 v[70:71], v128 offset:26624
	ds_read_b64_tr_b16 v[72:73], v128 offset:27648
	s_waitcnt lgkmcnt(12)
	v_mfma_f32_32x32x16_f16 v[82:97], v[194:197], v[150:153], v[82:97]
	v_add_f32_e32 v66, v80, v66
	v_add_f32_e32 v251, v81, v251
	v_add_f32_e32 v66, v50, v66
	v_add_f32_e32 v74, v51, v66
	v_cvt_pk_f16_f32 v168, v78, v79
	v_cvt_pk_f16_f32 v169, v80, v81
	ds_read_b64_tr_b16 v[66:67], v126 offset:28672
	ds_read_b64_tr_b16 v[68:69], v126 offset:29696
	s_waitcnt lgkmcnt(13)
	v_mfma_f32_32x32x16_f16 v[98:113], v[190:193], v[154:157], v[98:113]
	v_add_f32_e32 v251, v52, v251
	v_add_f32_e32 v74, v53, v74
	v_add_f32_e32 v251, v54, v251
	v_add_f32_e32 v74, v55, v74
	v_cvt_pk_f16_f32 v170, v50, v51
	v_cvt_pk_f16_f32 v171, v52, v53
	ds_read_b64_tr_b16 v[50:51], v128 offset:28672
	ds_read_b64_tr_b16 v[52:53], v128 offset:29696
	s_waitcnt lgkmcnt(14)
	v_mfma_f32_32x32x16_f16 v[82:97], v[186:189], v[154:157], v[82:97]
	v_add_f32_e32 v251, v56, v251
	v_add_f32_e32 v74, v57, v74
	v_add_f32_e32 v251, v58, v251
	v_add_f32_e32 v74, v59, v74
	v_cvt_pk_f16_f32 v172, v54, v55
	v_cvt_pk_f16_f32 v173, v56, v57
	ds_read_b64_tr_b16 v[54:55], v126 offset:30720
	ds_read_b64_tr_b16 v[56:57], v126 offset:31744
	s_waitcnt lgkmcnt(14)
	v_mfma_f32_32x32x16_f16 v[98:113], v[182:185], v[158:161], v[98:113]
	v_add_f32_e32 v251, v60, v251
	v_add_f32_e32 v74, v61, v74
	v_add_f32_e32 v251, v62, v251
	v_add_f32_e32 v74, v63, v74
	v_cvt_pk_f16_f32 v174, v58, v59
	v_cvt_pk_f16_f32 v175, v60, v61
	ds_read_b64_tr_b16 v[58:59], v128 offset:30720
	ds_read_b64_tr_b16 v[60:61], v128 offset:31744
	v_mfma_f32_32x32x16_f16 v[82:97], v[178:181], v[158:161], v[82:97]
	v_add_f32_e32 v251, v64, v251
	v_add_f32_e32 v74, v65, v74
	v_add_f32_e32 v74, v251, v74
	v_cvt_pk_f16_f32 v176, v62, v63
	v_cvt_pk_f16_f32 v177, v64, v65
	v_max_f32_e32 v62, v99, v98
	s_nop 5
	v_max3_f32 v63, v100, v101, v83
	v_max3_f32 v62, v62, v82, v84
	v_max3_f32 v62, v62, v85, v102
	v_max3_f32 v63, v63, v104, v105
	v_max3_f32 v62, v62, v103, v86
	v_max3_f32 v63, v63, v88, v89
	v_max3_f32 v62, v62, v87, v106
	v_max3_f32 v63, v63, v108, v109
	v_max3_f32 v62, v62, v107, v90
	v_max3_f32 v63, v63, v92, v93
	v_max3_f32 v62, v62, v91, v110
	v_max3_f32 v63, v63, v112, v113
	v_max3_f32 v62, v62, v111, v94
	v_max3_f32 v63, v63, v96, v97
	v_max3_f32 v62, v62, v95, v63
	v_mov_b32_e32 v63, v62
	s_nop 1
	v_permlane32_swap_b32_e32 v62, v63
	v_max_f32_e32 v62, v63, v62
	v_cmp_lt_f32_e32 vcc, s34, v62
	s_cmp_lg_u64 vcc, 0
	v_add_f32_e32 v182, v127, v74
	s_cselect_b64 s[8:9], -1, 0
	s_cbranch_vccnz .LBB1_25

.LBB1_10:
	v_mad_i64_i32 v[50:51], s[16:17], s19, v244, v[222:223]
	s_add_i32 s16, s35, s30
	s_add_i32 s20, s38, 1
	s_mov_b32 m0, s16
	s_nop 0
	global_load_lds_dwordx4 v[50:51], off
	s_addk_i32 s16, 0x1000
	s_cmp_ge_i32 s20, s29
	v_lshl_add_u64 v[50:51], v[50:51], 0, s[10:11]
	s_mov_b32 m0, s16
	s_nop 0
	global_load_lds_dwordx4 v[50:51], off
	s_cselect_b32 s16, s29, 0
	s_sub_i32 s19, 0, s16
	s_and_b64 s[16:17], s[6:7], exec
	s_cselect_b32 s16, s19, s28
	s_add_i32 s16, s16, s18
	s_add_i32 s16, s16, -3
	v_mad_i64_i32 v[50:51], s[16:17], s16, v244, v[224:225]
	s_add_i32 s16, s36, s31
	s_mov_b32 m0, s16
	s_nop 0
	global_load_lds_dwordx4 v[50:51], off
	v_lshl_add_u64 v[50:51], v[50:51], 0, s[10:11]
	s_addk_i32 s16, 0x1000
	s_mov_b32 m0, s16
	s_nop 0
	global_load_lds_dwordx4 v[50:51], off
	s_waitcnt vmcnt(4) lgkmcnt(0)
	s_barrier
	s_andn2_b64 vcc, exec, s[8:9]
	s_cbranch_vccnz .LBB1_12
	v_add_u32_e32 v66, s24, v233
	ds_read_b128 v[50:53], v66 offset:96
	ds_read_b128 v[54:57], v66 offset:64
	ds_read_b128 v[58:61], v66 offset:32
	ds_read_b128 v[66:69], v66
	s_waitcnt lgkmcnt(3)
	v_pk_mul_f32 v[46:47], v[46:47], v[50:51]
	s_waitcnt lgkmcnt(2)
	v_pk_mul_f32 v[42:43], v[42:43], v[54:55]
	s_waitcnt lgkmcnt(1)
	v_pk_mul_f32 v[38:39], v[38:39], v[58:59]
	v_pk_mul_f32 v[48:49], v[48:49], v[52:53]
	v_pk_mul_f32 v[44:45], v[44:45], v[56:57]
	v_pk_mul_f32 v[40:41], v[40:41], v[60:61]
	s_waitcnt lgkmcnt(0)
	v_pk_mul_f32 v[36:37], v[36:37], v[68:69]
	v_pk_mul_f32 v[34:35], v[34:35], v[66:67]
	v_pk_mul_f32 v[30:31], v[30:31], v[50:51]
	v_pk_mul_f32 v[26:27], v[26:27], v[54:55]
	v_pk_mul_f32 v[22:23], v[22:23], v[58:59]
	v_pk_mul_f32 v[32:33], v[32:33], v[52:53]
	v_pk_mul_f32 v[28:29], v[28:29], v[56:57]
	v_pk_mul_f32 v[24:25], v[24:25], v[60:61]
	v_pk_mul_f32 v[20:21], v[20:21], v[68:69]
	v_pk_mul_f32 v[18:19], v[18:19], v[66:67]
.LBB1_12:
	v_add_u32_e32 v174, s35, v240
	ds_read_b64_tr_b16 v[134:135], v174 offset:24576
	ds_read_b64_tr_b16 v[136:137], v174 offset:25600
	s_waitcnt lgkmcnt(9)
	v_mfma_f32_32x32x16_f16 v[66:81], v[62:65], v[146:149], v[2:17]
	v_add_f32_e32 v50, v98, v99
	v_mov_b32_e32 v251, v100
	v_add_f32_e32 v50, v101, v50
	v_add_f32_e32 v251, v102, v251
	v_add_f32_e32 v50, v103, v50
	v_cvt_pk_f16_f32 v162, v98, v99
	v_cvt_pk_f16_f32 v163, v100, v101
	v_add_u32_e32 v183, s35, v239
	ds_read_b64_tr_b16 v[142:143], v183 offset:24576
	ds_read_b64_tr_b16 v[144:145], v183 offset:25600
	v_add_f32_e32 v251, v104, v251
	v_add_f32_e32 v50, v105, v50
	v_add_f32_e32 v251, v106, v251
	v_add_f32_e32 v98, v107, v50
	s_waitcnt lgkmcnt(10)
	v_mfma_f32_32x32x16_f16 v[50:65], v[138:141], v[146:149], v[2:17]
	v_cvt_pk_f16_f32 v164, v102, v103
	v_cvt_pk_f16_f32 v165, v104, v105
	ds_read_b64_tr_b16 v[138:139], v174 offset:26624
	ds_read_b64_tr_b16 v[140:141], v174 offset:27648
	s_waitcnt lgkmcnt(11)
	v_mfma_f32_32x32x16_f16 v[66:81], v[178:181], v[150:153], v[66:81]
	v_add_f32_e32 v251, v108, v251
	v_add_f32_e32 v98, v109, v98
	v_add_f32_e32 v251, v110, v251
	v_add_f32_e32 v98, v111, v98
	v_cvt_pk_f16_f32 v166, v106, v107
	v_cvt_pk_f16_f32 v167, v108, v109
	ds_read_b64_tr_b16 v[102:103], v183 offset:26624
	ds_read_b64_tr_b16 v[104:105], v183 offset:27648
	s_waitcnt lgkmcnt(12)
	v_mfma_f32_32x32x16_f16 v[50:65], v[126:129], v[150:153], v[50:65]
	v_add_f32_e32 v251, v112, v251
	v_add_f32_e32 v98, v113, v98
	v_add_f32_e32 v251, v82, v251
	v_add_f32_e32 v106, v83, v98
	v_cvt_pk_f16_f32 v168, v110, v111
	v_cvt_pk_f16_f32 v169, v112, v113
	ds_read_b64_tr_b16 v[98:99], v174 offset:28672
	ds_read_b64_tr_b16 v[100:101], v174 offset:29696
	s_waitcnt lgkmcnt(13)
	v_mfma_f32_32x32x16_f16 v[66:81], v[130:133], v[154:157], v[66:81]
	v_add_f32_e32 v251, v84, v251
	v_add_f32_e32 v106, v85, v106
	v_add_f32_e32 v251, v86, v251
	v_add_f32_e32 v106, v87, v106
	v_cvt_pk_f16_f32 v170, v82, v83
	v_cvt_pk_f16_f32 v171, v84, v85
	ds_read_b64_tr_b16 v[82:83], v183 offset:28672
	ds_read_b64_tr_b16 v[84:85], v183 offset:29696
	s_waitcnt lgkmcnt(14)
	v_mfma_f32_32x32x16_f16 v[50:65], v[118:121], v[154:157], v[50:65]
	v_add_f32_e32 v251, v88, v251
	v_add_f32_e32 v106, v89, v106
	v_add_f32_e32 v251, v90, v251
	v_add_f32_e32 v106, v91, v106
	v_cvt_pk_f16_f32 v172, v86, v87
	v_cvt_pk_f16_f32 v173, v88, v89
	ds_read_b64_tr_b16 v[86:87], v174 offset:30720
	ds_read_b64_tr_b16 v[88:89], v174 offset:31744
	s_waitcnt lgkmcnt(14)
	v_mfma_f32_32x32x16_f16 v[66:81], v[122:125], v[158:161], v[66:81]
	v_add_f32_e32 v251, v92, v251
	v_add_f32_e32 v106, v93, v106
	v_add_f32_e32 v251, v94, v251
	v_add_f32_e32 v106, v95, v106
	v_cvt_pk_f16_f32 v174, v90, v91
	v_cvt_pk_f16_f32 v175, v92, v93
	ds_read_b64_tr_b16 v[90:91], v183 offset:30720
	ds_read_b64_tr_b16 v[92:93], v183 offset:31744
	v_mfma_f32_32x32x16_f16 v[50:65], v[114:117], v[158:161], v[50:65]
	v_add_f32_e32 v251, v96, v251
	v_add_f32_e32 v106, v97, v106
	v_add_f32_e32 v106, v251, v106
	v_cvt_pk_f16_f32 v176, v94, v95
	v_cvt_pk_f16_f32 v177, v96, v97
	v_max_f32_e32 v94, v67, v66
	s_nop 5
	v_max3_f32 v95, v68, v69, v51
	v_max3_f32 v94, v94, v50, v52
	v_max3_f32 v94, v94, v53, v70
	v_max3_f32 v95, v95, v72, v73
	v_max3_f32 v94, v94, v71, v54
	v_max3_f32 v95, v95, v56, v57
	v_max3_f32 v94, v94, v55, v74
	v_max3_f32 v95, v95, v76, v77
	v_max3_f32 v94, v94, v75, v58
	v_max3_f32 v95, v95, v60, v61
	v_max3_f32 v94, v94, v59, v78
	v_max3_f32 v95, v95, v80, v81
	v_max3_f32 v94, v94, v79, v62
	v_max3_f32 v95, v95, v64, v65
	v_max3_f32 v94, v94, v63, v95
	v_mov_b32_e32 v95, v94
	s_nop 1
	v_permlane32_swap_b32_e32 v94, v95
	v_max_f32_e32 v94, v95, v94
	v_cmp_lt_f32_e32 vcc, s34, v94
	s_cmp_lg_u64 vcc, 0
	v_add_f32_e32 v127, v182, v106
	s_cselect_b64 s[8:9], -1, 0
	s_cbranch_vccnz .LBB1_28

.LBB1_17:
	v_mad_i64_i32 v[82:83], s[16:17], s19, v244, v[222:223]
	s_add_i32 s16, s36, s30
	s_mov_b32 m0, s16
	s_nop 0
	global_load_lds_dwordx4 v[82:83], off
	v_lshl_add_u64 v[82:83], v[82:83], 0, s[10:11]
	s_addk_i32 s16, 0x1000
	s_mov_b32 m0, s16
	s_nop 0
	global_load_lds_dwordx4 v[82:83], off
	s_and_b64 vcc, exec, s[4:5]
	s_mov_b64 s[4:5], -1
	s_cbranch_vccnz .LBB1_19
	s_sub_i32 s4, s38, s27
	s_add_i32 s16, s4, 33
	s_mov_b64 s[4:5], 0

.LBB1_21:
	v_mad_i64_i32 v[82:83], s[4:5], s16, v244, v[224:225]
	s_add_i32 s4, s35, s31
	s_mov_b32 m0, s4
	s_nop 0
	global_load_lds_dwordx4 v[82:83], off
	v_lshl_add_u64 v[82:83], v[82:83], 0, s[10:11]
	s_addk_i32 s4, 0x1000
	s_mov_b32 m0, s4
	s_nop 0
	global_load_lds_dwordx4 v[82:83], off
	s_waitcnt vmcnt(4) lgkmcnt(0)
	s_barrier
	s_andn2_b64 vcc, exec, s[8:9]
	s_cbranch_vccnz .LBB1_23
	v_add_u32_e32 v94, s24, v233
	ds_read_b128 v[82:85], v94 offset:96
	ds_read_b128 v[86:89], v94 offset:64
	ds_read_b128 v[90:93], v94
	ds_read_b128 v[94:97], v94 offset:32
	s_waitcnt lgkmcnt(3)
	v_pk_mul_f32 v[48:49], v[48:49], v[84:85]
	v_pk_mul_f32 v[46:47], v[46:47], v[82:83]
	s_waitcnt lgkmcnt(2)
	v_pk_mul_f32 v[44:45], v[44:45], v[88:89]
	v_pk_mul_f32 v[42:43], v[42:43], v[86:87]
	s_waitcnt lgkmcnt(0)
	v_pk_mul_f32 v[40:41], v[40:41], v[96:97]
	v_pk_mul_f32 v[38:39], v[38:39], v[94:95]
	v_pk_mul_f32 v[36:37], v[36:37], v[92:93]
	v_pk_mul_f32 v[34:35], v[34:35], v[90:91]
	v_pk_mul_f32 v[32:33], v[32:33], v[84:85]
	v_pk_mul_f32 v[30:31], v[30:31], v[82:83]
	v_pk_mul_f32 v[28:29], v[28:29], v[88:89]
	v_pk_mul_f32 v[26:27], v[26:27], v[86:87]
	v_pk_mul_f32 v[24:25], v[24:25], v[96:97]
	v_pk_mul_f32 v[22:23], v[22:23], v[94:95]
	v_pk_mul_f32 v[20:21], v[20:21], v[92:93]
	v_pk_mul_f32 v[18:19], v[18:19], v[90:91]

.LBB1_35:
	s_cmp_lt_i32 s39, 31
	v_add_u32_e32 v114, s5, v240
	ds_read_b64_tr_b16 v[218:219], v114 offset:24576
	ds_read_b64_tr_b16 v[220:221], v114 offset:25600
	s_waitcnt vmcnt(3) lgkmcnt(9)
	v_mfma_f32_32x32x16_f16 v[98:113], v[206:209], v[146:149], v[2:17]
	v_add_f32_e32 v82, v66, v67
	v_add_f32_e32 v82, v68, v82
	v_add_f32_e32 v82, v69, v82
	v_add_f32_e32 v82, v70, v82
	v_add_f32_e32 v82, v71, v82
	v_cvt_pk_f16_f32 v162, v66, v67
	v_cvt_pk_f16_f32 v163, v68, v69
	v_add_u32_e32 v115, s5, v239
	ds_read_b64_tr_b16 v[214:215], v115 offset:24576
	ds_read_b64_tr_b16 v[216:217], v115 offset:25600
	v_add_f32_e32 v66, v72, v82
	s_waitcnt lgkmcnt(10)
	v_mfma_f32_32x32x16_f16 v[82:97], v[202:205], v[146:149], v[2:17]
	v_add_f32_e32 v66, v73, v66
	v_add_f32_e32 v66, v74, v66
	v_add_f32_e32 v66, v75, v66
	v_cvt_pk_f16_f32 v164, v70, v71
	v_cvt_pk_f16_f32 v165, v72, v73
	ds_read_b64_tr_b16 v[210:211], v114 offset:26624
	ds_read_b64_tr_b16 v[212:213], v114 offset:27648
	s_waitcnt vmcnt(2) lgkmcnt(11)
	v_mfma_f32_32x32x16_f16 v[98:113], v[198:201], v[150:153], v[98:113]
	v_add_f32_e32 v66, v76, v66
	v_add_f32_e32 v66, v77, v66
	v_add_f32_e32 v66, v78, v66
	v_add_f32_e32 v66, v79, v66
	v_cvt_pk_f16_f32 v166, v74, v75
	v_cvt_pk_f16_f32 v167, v76, v77
	ds_read_b64_tr_b16 v[70:71], v115 offset:26624
	ds_read_b64_tr_b16 v[72:73], v115 offset:27648
	s_waitcnt lgkmcnt(12)
	v_mfma_f32_32x32x16_f16 v[82:97], v[194:197], v[150:153], v[82:97]
	v_add_f32_e32 v66, v80, v66
	v_add_f32_e32 v66, v81, v66
	v_add_f32_e32 v66, v50, v66
	v_add_f32_e32 v74, v51, v66
	v_cvt_pk_f16_f32 v168, v78, v79
	v_cvt_pk_f16_f32 v169, v80, v81
	ds_read_b64_tr_b16 v[66:67], v114 offset:28672
	ds_read_b64_tr_b16 v[68:69], v114 offset:29696
	s_waitcnt vmcnt(1) lgkmcnt(13)
	v_mfma_f32_32x32x16_f16 v[98:113], v[190:193], v[154:157], v[98:113]
	v_add_f32_e32 v74, v52, v74
	v_add_f32_e32 v74, v53, v74
	v_add_f32_e32 v74, v54, v74
	v_add_f32_e32 v74, v55, v74
	v_cvt_pk_f16_f32 v170, v50, v51
	v_cvt_pk_f16_f32 v171, v52, v53
	ds_read_b64_tr_b16 v[50:51], v115 offset:28672
	ds_read_b64_tr_b16 v[52:53], v115 offset:29696
	s_waitcnt lgkmcnt(14)
	v_mfma_f32_32x32x16_f16 v[82:97], v[186:189], v[154:157], v[82:97]
	v_add_f32_e32 v74, v56, v74
	v_add_f32_e32 v74, v57, v74
	v_add_f32_e32 v74, v58, v74
	v_add_f32_e32 v74, v59, v74
	v_cvt_pk_f16_f32 v172, v54, v55
	v_cvt_pk_f16_f32 v173, v56, v57
	ds_read_b64_tr_b16 v[54:55], v114 offset:30720
	ds_read_b64_tr_b16 v[56:57], v114 offset:31744
	s_waitcnt vmcnt(0) lgkmcnt(14)
	v_mfma_f32_32x32x16_f16 v[98:113], v[182:185], v[158:161], v[98:113]
	v_add_f32_e32 v74, v60, v74
	v_add_f32_e32 v74, v61, v74
	v_add_f32_e32 v74, v62, v74
	v_add_f32_e32 v74, v63, v74
	v_cvt_pk_f16_f32 v174, v58, v59
	v_cvt_pk_f16_f32 v175, v60, v61
	ds_read_b64_tr_b16 v[58:59], v115 offset:30720
	ds_read_b64_tr_b16 v[60:61], v115 offset:31744
	v_mfma_f32_32x32x16_f16 v[82:97], v[178:181], v[158:161], v[82:97]
	v_add_f32_e32 v74, v64, v74
	v_add_f32_e32 v74, v65, v74
	v_add_f32_e32 v74, 0, v74
	v_cvt_pk_f16_f32 v176, v62, v63
	v_cvt_pk_f16_f32 v177, v64, v65
	s_cbranch_scc1 .LBB1_37
	v_lshl_add_u32 v62, s39, 6, v242
	v_or_b32_e32 v63, 32, v62
	v_cmp_le_u32_e32 vcc, v63, v241
	v_or_b32_e32 v63, 33, v62
	s_nop 2
	v_cndmask_b32_e32 v82, v245, v82, vcc
	v_cmp_lt_u32_e32 vcc, v62, v241
	s_nop 1
	v_cndmask_b32_e32 v99, v245, v99, vcc
	v_cmp_le_u32_e32 vcc, v62, v241
	s_nop 1
	v_cndmask_b32_e32 v98, v245, v98, vcc
	v_cmp_le_u32_e32 vcc, v63, v241
	v_or_b32_e32 v63, 2, v62
	s_nop 0
	v_cndmask_b32_e32 v83, v245, v83, vcc
	v_cmp_le_u32_e32 vcc, v63, v241
	v_or_b32_e32 v63, 34, v62
	s_nop 0
	v_cndmask_b32_e32 v100, v245, v100, vcc
	v_cmp_le_u32_e32 vcc, v63, v241
	v_or_b32_e32 v63, 3, v62
	s_nop 0
	v_cndmask_b32_e32 v84, v245, v84, vcc
	v_cmp_le_u32_e32 vcc, v63, v241
	v_or_b32_e32 v63, 35, v62
	s_nop 0
	v_cndmask_b32_e32 v101, v245, v101, vcc
	v_cmp_le_u32_e32 vcc, v63, v241
	v_or_b32_e32 v63, 8, v62
	s_nop 0
	v_cndmask_b32_e32 v85, v245, v85, vcc
	v_cmp_le_u32_e32 vcc, v63, v241
	v_or_b32_e32 v63, 40, v62
	s_nop 0
	v_cndmask_b32_e32 v102, v245, v102, vcc
	v_cmp_le_u32_e32 vcc, v63, v241
	v_or_b32_e32 v63, 9, v62
	s_nop 0
	v_cndmask_b32_e32 v86, v245, v86, vcc
	v_cmp_le_u32_e32 vcc, v63, v241
	v_or_b32_e32 v63, 41, v62
	s_nop 0
	v_cndmask_b32_e32 v103, v245, v103, vcc
	v_cmp_le_u32_e32 vcc, v63, v241
	v_or_b32_e32 v63, 10, v62
	s_nop 0
	v_cndmask_b32_e32 v87, v245, v87, vcc
	v_cmp_le_u32_e32 vcc, v63, v241
	v_or_b32_e32 v63, 42, v62
	s_nop 0
	v_cndmask_b32_e32 v104, v245, v104, vcc
	v_cmp_le_u32_e32 vcc, v63, v241
	v_or_b32_e32 v63, 11, v62
	s_nop 0
	v_cndmask_b32_e32 v88, v245, v88, vcc
	v_cmp_le_u32_e32 vcc, v63, v241
	v_or_b32_e32 v63, 43, v62
	s_nop 0
	v_cndmask_b32_e32 v105, v245, v105, vcc
	v_cmp_le_u32_e32 vcc, v63, v241
	v_or_b32_e32 v63, 16, v62
	s_nop 0
	v_cndmask_b32_e32 v89, v245, v89, vcc
	v_cmp_le_u32_e32 vcc, v63, v241
	v_or_b32_e32 v63, 48, v62
	s_nop 0
	v_cndmask_b32_e32 v106, v245, v106, vcc
	v_cmp_le_u32_e32 vcc, v63, v241
	v_or_b32_e32 v63, 17, v62
	s_nop 0
	v_cndmask_b32_e32 v90, v245, v90, vcc
	v_cmp_le_u32_e32 vcc, v63, v241
	v_or_b32_e32 v63, 49, v62
	s_nop 0
	v_cndmask_b32_e32 v107, v245, v107, vcc
	v_cmp_le_u32_e32 vcc, v63, v241
	v_or_b32_e32 v63, 18, v62
	s_nop 0
	v_cndmask_b32_e32 v91, v245, v91, vcc
	v_cmp_le_u32_e32 vcc, v63, v241
	v_or_b32_e32 v63, 50, v62
	s_nop 0
	v_cndmask_b32_e32 v108, v245, v108, vcc
	v_cmp_le_u32_e32 vcc, v63, v241
	v_or_b32_e32 v63, 19, v62
	s_nop 0
	v_cndmask_b32_e32 v92, v245, v92, vcc
	v_cmp_le_u32_e32 vcc, v63, v241
	v_or_b32_e32 v63, 51, v62
	s_nop 0
	v_cndmask_b32_e32 v109, v245, v109, vcc
	v_cmp_le_u32_e32 vcc, v63, v241
	v_or_b32_e32 v63, 24, v62
	s_nop 0
	v_cndmask_b32_e32 v93, v245, v93, vcc
	v_cmp_le_u32_e32 vcc, v63, v241
	v_or_b32_e32 v63, 56, v62
	s_nop 0
	v_cndmask_b32_e32 v110, v245, v110, vcc
	v_cmp_le_u32_e32 vcc, v63, v241
	v_or_b32_e32 v63, 25, v62
	s_nop 0
	v_cndmask_b32_e32 v94, v245, v94, vcc
	v_cmp_le_u32_e32 vcc, v63, v241
	v_or_b32_e32 v63, 57, v62
	s_nop 0
	v_cndmask_b32_e32 v111, v245, v111, vcc
	v_cmp_le_u32_e32 vcc, v63, v241
	v_or_b32_e32 v63, 26, v62
	s_nop 0
	v_cndmask_b32_e32 v95, v245, v95, vcc
	v_cmp_le_u32_e32 vcc, v63, v241
	v_or_b32_e32 v63, 58, v62
	s_nop 0
	v_cndmask_b32_e32 v112, v245, v112, vcc
	v_cmp_le_u32_e32 vcc, v63, v241
	v_or_b32_e32 v63, 27, v62
	v_or_b32_e32 v62, 59, v62
	v_cndmask_b32_e32 v96, v245, v96, vcc
	v_cmp_le_u32_e32 vcc, v63, v241
	s_nop 1
	v_cndmask_b32_e32 v113, v245, v113, vcc
	v_cmp_le_u32_e32 vcc, v62, v241
	s_nop 1
	v_cndmask_b32_e32 v97, v245, v97, vcc

.LBB1_49:
	s_waitcnt lgkmcnt(4)
	v_mfma_f32_32x32x16_f16 v[18:33], v[170:173], v[50:53], v[18:33]
	v_exp_f32_e32 v118, v118
	v_exp_f32_e32 v119, v119
	v_exp_f32_e32 v120, v120
	v_exp_f32_e32 v121, v121
	s_waitcnt lgkmcnt(2)
	v_mfma_f32_32x32x16_f16 v[34:49], v[174:177], v[54:57], v[34:49]
	v_exp_f32_e32 v122, v122
	v_exp_f32_e32 v123, v123
	v_exp_f32_e32 v124, v124
	v_exp_f32_e32 v125, v125
	s_waitcnt lgkmcnt(0)
	v_mfma_f32_32x32x16_f16 v[18:33], v[174:177], v[58:61], v[18:33]
	v_exp_f32_e32 v126, v126
	v_exp_f32_e32 v127, v127
	v_exp_f32_e32 v128, v128
	v_exp_f32_e32 v129, v129
	s_cmp_gt_i32 s39, 29
	s_cselect_b64 s[20:21], -1, 0
	s_and_b64 vcc, exec, s[20:21]
	s_cbranch_vccnz .LBB1_51
	s_add_i32 s36, s39, 3
	s_cmp_ge_i32 s36, s29
	s_cselect_b32 s38, s29, 0
	s_sub_i32 s38, 0, s38
	s_and_b64 s[40:41], s[6:7], exec
	s_cselect_b32 s38, s38, s28
	s_add_i32 s38, s38, s36
	v_mad_i64_i32 v[50:51], s[40:41], s38, v244, v[222:223]
	s_add_i32 s36, s35, s30
	s_mov_b32 m0, s36
	s_nop 0
	global_load_lds_dwordx4 v[50:51], off
	v_lshl_add_u64 v[50:51], v[50:51], 0, s[10:11]
	s_addk_i32 s36, 0x1000
	s_mov_b32 m0, s36
	s_nop 0
	global_load_lds_dwordx4 v[50:51], off
.LBB1_51:
	s_and_b64 vcc, exec, s[4:5]
	s_cbranch_vccnz .LBB1_53
	s_add_i32 s36, s39, 1
	s_cmp_ge_i32 s36, s29
	s_cselect_b32 s4, s29, 0
	s_sub_i32 s38, 0, s4
	s_and_b64 s[4:5], s[6:7], exec
	s_cselect_b32 s4, s38, s28
	s_add_i32 s4, s4, s36
	v_mad_i64_i32 v[50:51], s[4:5], s4, v244, v[224:225]
	s_add_i32 s4, s37, s31
	s_mov_b32 m0, s4
	s_nop 0
	global_load_lds_dwordx4 v[50:51], off
	v_lshl_add_u64 v[50:51], v[50:51], 0, s[10:11]
	s_addk_i32 s4, 0x1000
	s_mov_b32 m0, s4
	s_nop 0
	global_load_lds_dwordx4 v[50:51], off

.LBB1_68:
	s_cmp_lt_i32 s39, 30
	v_add_u32_e32 v24, s35, v240
	ds_read_b64_tr_b16 v[42:43], v24 offset:24576
	ds_read_b64_tr_b16 v[44:45], v24 offset:25600
	v_mfma_f32_32x32x16_f16 v[66:81], v[206:209], v[146:149], v[2:17]
	v_add_f32_e32 v18, v130, v131
	v_add_f32_e32 v18, v132, v18
	v_add_f32_e32 v18, v133, v18
	v_add_f32_e32 v18, v134, v18
	v_add_f32_e32 v18, v135, v18
	v_cvt_pk_f16_f32 v162, v130, v131
	v_cvt_pk_f16_f32 v163, v132, v133
	v_add_u32_e32 v28, s35, v239
	ds_read_b64_tr_b16 v[46:47], v28 offset:24576
	ds_read_b64_tr_b16 v[48:49], v28 offset:25600
	v_mfma_f32_32x32x16_f16 v[50:65], v[202:205], v[146:149], v[2:17]
	v_add_f32_e32 v18, v136, v18
	v_add_f32_e32 v18, v137, v18
	v_add_f32_e32 v18, v138, v18
	v_add_f32_e32 v18, v139, v18
	v_cvt_pk_f16_f32 v164, v134, v135
	v_cvt_pk_f16_f32 v165, v136, v137
	ds_read_b64_tr_b16 v[38:39], v24 offset:26624
	ds_read_b64_tr_b16 v[40:41], v24 offset:27648
	v_mfma_f32_32x32x16_f16 v[66:81], v[198:201], v[150:153], v[66:81]
	v_add_f32_e32 v18, v140, v18
	v_add_f32_e32 v18, v141, v18
	v_add_f32_e32 v18, v142, v18
	v_add_f32_e32 v18, v143, v18
	v_cvt_pk_f16_f32 v166, v138, v139
	v_cvt_pk_f16_f32 v167, v140, v141
	ds_read_b64_tr_b16 v[34:35], v28 offset:26624
	ds_read_b64_tr_b16 v[36:37], v28 offset:27648
	v_mfma_f32_32x32x16_f16 v[50:65], v[194:197], v[150:153], v[50:65]
	v_add_f32_e32 v18, v144, v18
	v_add_f32_e32 v18, v145, v18
	v_add_f32_e32 v18, v114, v18
	v_add_f32_e32 v18, v115, v18
	v_cvt_pk_f16_f32 v168, v142, v143
	v_cvt_pk_f16_f32 v169, v144, v145
	ds_read_b64_tr_b16 v[30:31], v24 offset:28672
	ds_read_b64_tr_b16 v[32:33], v24 offset:29696
	v_mfma_f32_32x32x16_f16 v[66:81], v[190:193], v[154:157], v[66:81]
	v_add_f32_e32 v18, v116, v18
	v_add_f32_e32 v18, v117, v18
	v_add_f32_e32 v18, v118, v18
	v_add_f32_e32 v22, v119, v18
	v_cvt_pk_f16_f32 v170, v114, v115
	v_cvt_pk_f16_f32 v171, v116, v117
	ds_read_b64_tr_b16 v[18:19], v28 offset:28672
	ds_read_b64_tr_b16 v[20:21], v28 offset:29696
	v_mfma_f32_32x32x16_f16 v[50:65], v[186:189], v[154:157], v[50:65]
	v_add_f32_e32 v22, v120, v22
	v_add_f32_e32 v22, v121, v22
	v_add_f32_e32 v22, v122, v22
	v_add_f32_e32 v26, v123, v22
	v_cvt_pk_f16_f32 v172, v118, v119
	v_cvt_pk_f16_f32 v173, v120, v121
	ds_read_b64_tr_b16 v[22:23], v24 offset:30720
	ds_read_b64_tr_b16 v[24:25], v24 offset:31744
	v_mfma_f32_32x32x16_f16 v[66:81], v[182:185], v[158:161], v[66:81]
	v_add_f32_e32 v26, v124, v26
	v_add_f32_e32 v26, v125, v26
	v_add_f32_e32 v26, v126, v26
	v_add_f32_e32 v114, v127, v26
	v_cvt_pk_f16_f32 v174, v122, v123
	v_cvt_pk_f16_f32 v175, v124, v125
	ds_read_b64_tr_b16 v[26:27], v28 offset:30720
	ds_read_b64_tr_b16 v[28:29], v28 offset:31744
	v_mfma_f32_32x32x16_f16 v[50:65], v[178:181], v[158:161], v[50:65]
	v_add_f32_e32 v114, v128, v114
	v_add_f32_e32 v114, v129, v114
	v_add_f32_e32 v114, 0, v114
	v_cvt_pk_f16_f32 v176, v126, v127
	v_cvt_pk_f16_f32 v177, v128, v129
	s_cbranch_scc1 .LBB1_70
	v_lshl_add_u32 v115, s39, 6, v243
	v_or_b32_e32 v116, 32, v115
	v_cmp_le_u32_e32 vcc, v116, v241
	v_or_b32_e32 v116, 33, v115
	s_nop 2
	v_cndmask_b32_e32 v50, v245, v50, vcc
	v_cmp_lt_u32_e32 vcc, v115, v241
	s_nop 1
	v_cndmask_b32_e32 v67, v245, v67, vcc
	v_cmp_le_u32_e32 vcc, v115, v241
	s_nop 1
	v_cndmask_b32_e32 v66, v245, v66, vcc
	v_cmp_le_u32_e32 vcc, v116, v241
	v_or_b32_e32 v116, 2, v115
	s_nop 0
	v_cndmask_b32_e32 v51, v245, v51, vcc
	v_cmp_le_u32_e32 vcc, v116, v241
	v_or_b32_e32 v116, 34, v115
	s_nop 0
	v_cndmask_b32_e32 v68, v245, v68, vcc
	v_cmp_le_u32_e32 vcc, v116, v241
	v_or_b32_e32 v116, 3, v115
	s_nop 0
	v_cndmask_b32_e32 v52, v245, v52, vcc
	v_cmp_le_u32_e32 vcc, v116, v241
	v_or_b32_e32 v116, 35, v115
	s_nop 0
	v_cndmask_b32_e32 v69, v245, v69, vcc
	v_cmp_le_u32_e32 vcc, v116, v241
	v_or_b32_e32 v116, 8, v115
	s_nop 0
	v_cndmask_b32_e32 v53, v245, v53, vcc
	v_cmp_le_u32_e32 vcc, v116, v241
	v_or_b32_e32 v116, 40, v115
	s_nop 0
	v_cndmask_b32_e32 v70, v245, v70, vcc
	v_cmp_le_u32_e32 vcc, v116, v241
	v_or_b32_e32 v116, 9, v115
	s_nop 0
	v_cndmask_b32_e32 v54, v245, v54, vcc
	v_cmp_le_u32_e32 vcc, v116, v241
	v_or_b32_e32 v116, 41, v115
	s_nop 0
	v_cndmask_b32_e32 v71, v245, v71, vcc
	v_cmp_le_u32_e32 vcc, v116, v241
	v_or_b32_e32 v116, 10, v115
	s_nop 0
	v_cndmask_b32_e32 v55, v245, v55, vcc
	v_cmp_le_u32_e32 vcc, v116, v241
	v_or_b32_e32 v116, 42, v115
	s_nop 0
	v_cndmask_b32_e32 v72, v245, v72, vcc
	v_cmp_le_u32_e32 vcc, v116, v241
	v_or_b32_e32 v116, 11, v115
	s_nop 0
	v_cndmask_b32_e32 v56, v245, v56, vcc
	v_cmp_le_u32_e32 vcc, v116, v241
	v_or_b32_e32 v116, 43, v115
	s_nop 0
	v_cndmask_b32_e32 v73, v245, v73, vcc
	v_cmp_le_u32_e32 vcc, v116, v241
	v_or_b32_e32 v116, 16, v115
	s_nop 0
	v_cndmask_b32_e32 v57, v245, v57, vcc
	v_cmp_le_u32_e32 vcc, v116, v241
	v_or_b32_e32 v116, 48, v115
	s_nop 0
	v_cndmask_b32_e32 v74, v245, v74, vcc
	v_cmp_le_u32_e32 vcc, v116, v241
	v_or_b32_e32 v116, 17, v115
	s_nop 0
	v_cndmask_b32_e32 v58, v245, v58, vcc
	v_cmp_le_u32_e32 vcc, v116, v241
	v_or_b32_e32 v116, 49, v115
	s_nop 0
	v_cndmask_b32_e32 v75, v245, v75, vcc
	v_cmp_le_u32_e32 vcc, v116, v241
	v_or_b32_e32 v116, 18, v115
	s_nop 0
	v_cndmask_b32_e32 v59, v245, v59, vcc
	v_cmp_le_u32_e32 vcc, v116, v241
	v_or_b32_e32 v116, 50, v115
	s_nop 0
	v_cndmask_b32_e32 v76, v245, v76, vcc
	v_cmp_le_u32_e32 vcc, v116, v241
	v_or_b32_e32 v116, 19, v115
	s_nop 0
	v_cndmask_b32_e32 v60, v245, v60, vcc
	v_cmp_le_u32_e32 vcc, v116, v241
	v_or_b32_e32 v116, 51, v115
	s_nop 0
	v_cndmask_b32_e32 v77, v245, v77, vcc
	v_cmp_le_u32_e32 vcc, v116, v241
	v_or_b32_e32 v116, 24, v115
	s_nop 0
	v_cndmask_b32_e32 v61, v245, v61, vcc
	v_cmp_le_u32_e32 vcc, v116, v241
	v_or_b32_e32 v116, 56, v115
	s_nop 0
	v_cndmask_b32_e32 v78, v245, v78, vcc
	v_cmp_le_u32_e32 vcc, v116, v241
	v_or_b32_e32 v116, 25, v115
	s_nop 0
	v_cndmask_b32_e32 v62, v245, v62, vcc
	v_cmp_le_u32_e32 vcc, v116, v241
	v_or_b32_e32 v116, 57, v115
	s_nop 0
	v_cndmask_b32_e32 v79, v245, v79, vcc
	v_cmp_le_u32_e32 vcc, v116, v241
	v_or_b32_e32 v116, 26, v115
	s_nop 0
	v_cndmask_b32_e32 v63, v245, v63, vcc
	v_cmp_le_u32_e32 vcc, v116, v241
	v_or_b32_e32 v116, 58, v115
	s_nop 0
	v_cndmask_b32_e32 v80, v245, v80, vcc
	v_cmp_le_u32_e32 vcc, v116, v241
	v_or_b32_e32 v116, 27, v115
	v_or_b32_e32 v115, 59, v115
	v_cndmask_b32_e32 v64, v245, v64, vcc
	v_cmp_le_u32_e32 vcc, v116, v241
	s_nop 1
	v_cndmask_b32_e32 v81, v245, v81, vcc
	v_cmp_le_u32_e32 vcc, v115, v241
	s_nop 1
	v_cndmask_b32_e32 v65, v245, v65, vcc

.LBB1_85:
	v_mad_i64_i32 v[18:19], s[20:21], s38, v244, v[222:223]
	s_add_i32 s20, s37, s30
	s_mov_b32 m0, s20
	s_nop 0
	global_load_lds_dwordx4 v[18:19], off
	v_lshl_add_u64 v[18:19], v[18:19], 0, s[10:11]
	s_addk_i32 s20, 0x1000
	s_mov_b32 m0, s20
	s_nop 0
	global_load_lds_dwordx4 v[18:19], off
.LBB1_86:
	s_and_b64 vcc, exec, s[4:5]
	s_add_i32 s38, s39, 2
	s_cbranch_vccnz .LBB1_88
	s_cmp_ge_i32 s38, s28
	s_cselect_b32 s4, s28, 0
	s_sub_i32 s20, 0, s4
	s_and_b64 s[4:5], s[6:7], exec
	s_cselect_b32 s4, s20, s28
	s_add_i32 s4, s4, s38
	v_mad_i64_i32 v[18:19], s[4:5], s4, v244, v[224:225]
	s_add_i32 s4, s36, s31
	s_mov_b32 m0, s4
	s_nop 0
	global_load_lds_dwordx4 v[18:19], off
	v_lshl_add_u64 v[18:19], v[18:19], 0, s[10:11]
	s_addk_i32 s4, 0x1000
	s_mov_b32 m0, s4
	s_nop 0
	global_load_lds_dwordx4 v[18:19], off

	.amdhsa_kernel _Z10attn64_fwdPKDF16_S0_S0_PDF16_
		.amdhsa_group_segment_fixed_size 0
		.amdhsa_private_segment_fixed_size 0
		.amdhsa_kernarg_size 32
		.amdhsa_user_sgpr_count 2
		.amdhsa_user_sgpr_dispatch_ptr 0
		.amdhsa_user_sgpr_queue_ptr 0
		.amdhsa_user_sgpr_kernarg_segment_ptr 1
		.amdhsa_user_sgpr_dispatch_id 0
		.amdhsa_user_sgpr_kernarg_preload_length 0
		.amdhsa_user_sgpr_kernarg_preload_offset 0
		.amdhsa_user_sgpr_private_segment_size 0
		.amdhsa_uses_dynamic_stack 0
		.amdhsa_enable_private_segment 0
		.amdhsa_system_sgpr_workgroup_id_x 1
		.amdhsa_system_sgpr_workgroup_id_y 0
		.amdhsa_system_sgpr_workgroup_id_z 0
		.amdhsa_system_sgpr_workgroup_info 0
		.amdhsa_system_vgpr_workitem_id 0
		.amdhsa_next_free_vgpr 252
		.amdhsa_next_free_sgpr 42
		.amdhsa_accum_offset 252
		.amdhsa_reserve_vcc 1
		.amdhsa_float_round_mode_32 0
		.amdhsa_float_round_mode_16_64 0
		.amdhsa_float_denorm_mode_32 3
		.amdhsa_float_denorm_mode_16_64 3
		.amdhsa_dx10_clamp 1
		.amdhsa_ieee_mode 1
		.amdhsa_fp16_overflow 0
		.amdhsa_tg_split 0
		.amdhsa_exception_fp_ieee_invalid_op 0
		.amdhsa_exception_fp_denorm_src 0
		.amdhsa_exception_fp_ieee_div_zero 0
		.amdhsa_exception_fp_ieee_overflow 0
		.amdhsa_exception_fp_ieee_underflow 0
		.amdhsa_exception_fp_ieee_inexact 0
		.amdhsa_exception_int_div_zero 0
	.end_amdhsa_kernel

amdhsa.kernels:
  - .agpr_count:     0
    .args:
      - .actual_access:  read_only
        .address_space:  global
        .offset:         0
        .size:           8
        .value_kind:     global_buffer
      - .actual_access:  read_only
        .address_space:  global
        .offset:         8
        .size:           8
        .value_kind:     global_buffer
      - .actual_access:  read_only
        .address_space:  global
        .offset:         16
        .size:           8
        .value_kind:     global_buffer
      - .actual_access:  read_only
        .address_space:  global
        .offset:         24
        .size:           8
        .value_kind:     global_buffer
      - .actual_access:  read_only
        .address_space:  global
        .offset:         32
        .size:           8
        .value_kind:     global_buffer
      - .address_space:  global
        .offset:         40
        .size:           8
        .value_kind:     global_buffer
      - .address_space:  global
        .offset:         48
        .size:           8
        .value_kind:     global_buffer
      - .address_space:  global
        .offset:         56
        .size:           8
        .value_kind:     global_buffer
      - .address_space:  global
        .offset:         64
        .size:           8
        .value_kind:     global_buffer
    .group_segment_fixed_size: 0
    .kernarg_segment_align: 8
    .kernarg_segment_size: 72
    .language:       OpenCL C
    .language_version:
      - 2
      - 0
    .max_flat_workgroup_size: 256
    .name:           _Z11prep_kernelPKfS0_S0_S0_S0_PDF16_S1_S1_P15HIP_vector_typeIfLj2EE
    .private_segment_fixed_size: 0
    .sgpr_count:     22
    .sgpr_spill_count: 0
    .symbol:         _Z11prep_kernelPKfS0_S0_S0_S0_PDF16_S1_S1_P15HIP_vector_typeIfLj2EE.kd
    .uniform_work_group_size: 1
    .uses_dynamic_stack: false
    .vgpr_count:     20
    .vgpr_spill_count: 0
    .wavefront_size: 64
  - .agpr_count:     0
    .args:
      - .address_space:  global
        .offset:         0
        .size:           8
        .value_kind:     global_buffer
      - .address_space:  global
        .offset:         8
        .size:           8
        .value_kind:     global_buffer
      - .address_space:  global
        .offset:         16
        .size:           8
        .value_kind:     global_buffer
      - .address_space:  global
        .offset:         24
        .size:           8
        .value_kind:     global_buffer
    .group_segment_fixed_size: 0
    .kernarg_segment_align: 8
    .kernarg_segment_size: 32
    .language:       OpenCL C
    .language_version:
      - 2
      - 0
    .max_flat_workgroup_size: 512
    .name:           _Z10attn64_fwdPKDF16_S0_S0_PDF16_
    .private_segment_fixed_size: 0
    .sgpr_count:     48
    .sgpr_spill_count: 0
    .symbol:         _Z10attn64_fwdPKDF16_S0_S0_PDF16_.kd
    .uniform_work_group_size: 1
    .uses_dynamic_stack: false
    .vgpr_count:     252
    .vgpr_spill_count: 0
    .wavefront_size: 64
  - .agpr_count:     0
    .args:
      - .address_space:  global
        .offset:         0
        .size:           8
        .value_kind:     global_buffer
      - .address_space:  global
        .offset:         8
        .size:           8
        .value_kind:     global_buffer
      - .address_space:  global
        .offset:         16
        .size:           8
        .value_kind:     global_buffer
      - .address_space:  global
        .offset:         24
        .size:           8
        .value_kind:     global_buffer
      - .address_space:  global
        .offset:         32
        .size:           8
        .value_kind:     global_buffer
      - .address_space:  global
        .offset:         40
        .size:           8
        .value_kind:     global_buffer
      - .actual_access:  read_only
        .address_space:  global
        .offset:         48
        .size:           8
        .value_kind:     global_buffer
      - .offset:         56
        .size:           4
        .value_kind:     by_value
      - .offset:         60
        .size:           4
        .value_kind:     by_value
      - .offset:         64
        .size:           4
        .value_kind:     by_value
    .group_segment_fixed_size: 0
    .kernarg_segment_align: 8
    .kernarg_segment_size: 68
    .language:       OpenCL C
    .language_version:
      - 2
      - 0
    .max_flat_workgroup_size: 768
    .name:           _Z7gemm_dbILi256ELi192ELi64ELi96ELi64ELi2ELi1ELi4EEvPKDF16_S1_PfPDF16_S3_S3_PK15HIP_vector_typeIfLj2EEiii
    .private_segment_fixed_size: 0
    .sgpr_count:     23
    .sgpr_spill_count: 0
    .symbol:         _Z7gemm_dbILi256ELi192ELi64ELi96ELi64ELi2ELi1ELi4EEvPKDF16_S1_PfPDF16_S3_S3_PK15HIP_vector_typeIfLj2EEiii.kd
    .uniform_work_group_size: 1
    .uses_dynamic_stack: false
    .vgpr_count:     137
    .vgpr_spill_count: 0
    .wavefront_size: 64
  - .agpr_count:     0
    .args:
      - .address_space:  global
        .offset:         0
        .size:           8
        .value_kind:     global_buffer
      - .address_space:  global
        .offset:         8
        .size:           8
        .value_kind:     global_buffer
      - .address_space:  global
        .offset:         16
        .size:           8
        .value_kind:     global_buffer
      - .address_space:  global
        .offset:         24
        .size:           8
        .value_kind:     global_buffer
      - .address_space:  global
        .offset:         32
        .size:           8
        .value_kind:     global_buffer
      - .address_space:  global
        .offset:         40
        .size:           8
        .value_kind:     global_buffer
      - .actual_access:  read_only
        .address_space:  global
        .offset:         48
        .size:           8
        .value_kind:     global_buffer
      - .offset:         56
        .size:           4
        .value_kind:     by_value
      - .offset:         60
        .size:           4
        .value_kind:     by_value
      - .offset:         64
        .size:           4
        .value_kind:     by_value
    .group_segment_fixed_size: 0
    .kernarg_segment_align: 8
    .kernarg_segment_size: 68
    .language:       OpenCL C
    .language_version:
      - 2
      - 0
    .max_flat_workgroup_size: 512
    .name:           _Z7gemm_dbILi128ELi128ELi64ELi64ELi64ELi3ELi0ELi4EEvPKDF16_S1_PfPDF16_S3_S3_PK15HIP_vector_typeIfLj2EEiii
    .private_segment_fixed_size: 0
    .sgpr_count:     26
    .sgpr_spill_count: 0
    .symbol:         _Z7gemm_dbILi128ELi128ELi64ELi64ELi64ELi3ELi0ELi4EEvPKDF16_S1_PfPDF16_S3_S3_PK15HIP_vector_typeIfLj2EEiii.kd
    .uniform_work_group_size: 1
    .uses_dynamic_stack: false
    .vgpr_count:     168
    .vgpr_spill_count: 0
    .wavefront_size: 64
